# GLA units: next-unit queue pop issued after the first loads, and the layer-0 unit tops no longer wait for the previous unit's stores before reusing their data registers (store data is read at issue)
# speedup vs baseline: 1.0060x; 1.0060x over previous
.LBB0_759:
	v_ashrrev_i32_e32 v18, 3, v39
	v_ashrrev_i32_e32 v19, 31, v18
	v_lshl_add_u64 v[2:3], s[22:23], 0, v[18:19]
	v_mad_u64_u32 v[4:5], s[4:5], v2, s27, v[16:17]
	v_mov_b32_e32 v2, v5
	s_and_b32 s55, s54, 3
	v_mad_u64_u32 v[2:3], s[4:5], v3, s27, v[2:3]
	v_and_b32_e32 v38, 7, v39
	v_mov_b32_e32 v5, v2
	s_lshl_b32 s16, s55, 7
	v_lshl_add_u64 v[2:3], v[4:5], 0, s[16:17]
	v_lshlrev_b32_e32 v14, 4, v38
	v_lshl_add_u64 v[2:3], v[2:3], 0, v[14:15]
	v_add_co_u32_e32 v20, vcc, s28, v2
	s_lshl_b32 s16, s55, 8
	s_nop 0
	v_addc_co_u32_e32 v21, vcc, 0, v3, vcc
	v_lshl_add_u64 v[2:3], v[4:5], 0, s[16:17]
	v_lshlrev_b32_e32 v14, 5, v38
	v_lshl_add_u64 v[2:3], v[2:3], 0, v[14:15]
	v_add_co_u32_e32 v24, vcc, 0x1000, v2
	v_lshl_add_u64 v[22:23], v[2:3], 0, s[18:19]
	s_nop 0
	v_addc_co_u32_e32 v25, vcc, 0, v3, vcc
	global_load_dwordx4 v[6:9], v[24:25], off offset:1536
	global_load_dwordx4 v[10:13], v[20:21], off offset:1024
	global_load_dwordx4 v[2:5], v[22:23], off offset:16
	v_cmp_gt_i32_e32 vcc, s29, v39
	s_and_saveexec_b64 s[24:25], vcc
	s_cbranch_execz .Lglr_pre0
	v_ashrrev_i32_e32 v24, 2, v39
	v_ashrrev_i32_e32 v25, 31, v24
	v_lshl_add_u64 v[20:21], s[22:23], 0, v[24:25]
	v_mad_u64_u32 v[22:23], s[22:23], v20, s27, v[16:17]
	v_mov_b32_e32 v14, v23
	v_mad_u64_u32 v[20:21], s[22:23], v21, s27, v[14:15]
	v_lshlrev_b32_e32 v14, 3, v39
	v_and_b32_e32 v19, 24, v14
	v_mov_b32_e32 v23, v20
	v_lshlrev_b32_e32 v14, 1, v19
	v_lshl_add_u64 v[20:21], v[22:23], 0, v[14:15]
	v_add_co_u32_e32 v20, vcc, s28, v20
	v_lshlrev_b32_e32 v14, 7, v24
	s_nop 0
	v_addc_co_u32_e32 v21, vcc, 0, v21, vcc
	global_load_dwordx4 v[20:23], v[20:21], off offset:3584
	v_lshlrev_b32_e32 v19, 2, v19
	v_add3_u32 v14, 0, v14, v19

.LBB0_1356:
	v_mov_b32_e32 v85, 0
	s_add_i32 s4, s85, 0xfffffce0
	s_mul_hi_i32 s5, s4, 0x3e0f83e1
	s_lshr_b32 s6, s5, 31
	s_ashr_i32 s67, s5, 5
	s_add_i32 s67, s67, s6
	s_mul_i32 s5, s67, 0x84
	s_sub_i32 s68, s4, s5
	s_ashr_i32 s4, s67, 2
	s_and_b32 s34, s67, 3
	s_cmp_lt_i32 s68, 4
	s_cselect_b64 s[6:7], -1, 0
	s_cmp_gt_i32 s68, 3
	s_cselect_b64 s[28:29], -1, 0
	s_ashr_i32 s5, s4, 31
	s_lshl_b32 s26, s4, 8
	s_lshl_b32 s14, s68, 6
	s_lshl_b64 s[24:25], s[4:5], 13
	s_ashr_i32 s27, s26, 31
	s_and_b64 s[4:5], s[6:7], exec
	s_cselect_b32 s4, s38, 0xffffff00
	s_cselect_b32 s5, s27, s25
	s_cselect_b32 s6, s26, s24
	s_add_i32 s4, s4, s14
	v_mov_b32 v87, v0
	s_add_u32 s26, s6, s4
	v_ashrrev_i32_e32 v18, 3, v87
	s_addc_u32 s27, s5, 0
	v_ashrrev_i32_e32 v19, 31, v18
	v_lshl_add_u64 v[2:3], s[26:27], 0, v[18:19]
	v_mad_u64_u32 v[4:5], s[4:5], v2, s39, v[76:77]
	v_and_b32_e32 v36, 7, v87
	v_mad_i32_i24 v5, v3, s39, v5
	s_lshl_b32 s14, s34, 7
	v_lshlrev_b32_e32 v74, 4, v36
	v_lshl_add_u64 v[2:3], v[4:5], 0, s[14:15]
	v_lshl_add_u64 v[2:3], v[2:3], 0, v[74:75]
	v_add_co_u32_e32 v2, vcc, s50, v2
	s_lshl_b32 s4, s34, 8
	s_nop 0
	v_addc_co_u32_e32 v3, vcc, 0, v3, vcc
	s_mov_b32 s5, s15
	global_load_dwordx4 v[14:17], v[2:3], off offset:512
	global_load_dwordx4 v[10:13], v[2:3], off offset:1024
	v_lshl_add_u64 v[2:3], v[4:5], 0, s[4:5]
	v_lshlrev_b32_e32 v74, 5, v36
	v_lshl_add_u64 v[2:3], v[2:3], 0, v[74:75]
	v_lshl_add_u64 v[4:5], v[2:3], 0, s[16:17]
	v_add_co_u32_e32 v2, vcc, 0x1000, v2
	v_readfirstlane_b32 s69, v87
	s_nop 0
	v_addc_co_u32_e32 v3, vcc, 0, v3, vcc
	global_load_dwordx4 v[6:9], v[2:3], off offset:1536
	s_nop 0
	global_load_dwordx4 v[2:5], v[4:5], off offset:16
	v_cmp_gt_i32_e32 vcc, s51, v87
	s_and_saveexec_b64 s[30:31], vcc
	s_cbranch_execz .Lglr_pre1
	v_ashrrev_i32_e32 v24, 2, v87
	v_ashrrev_i32_e32 v25, 31, v24
	v_lshl_add_u64 v[20:21], s[26:27], 0, v[24:25]
	v_mad_u64_u32 v[22:23], s[70:71], v20, s39, v[76:77]
	v_mov_b32_e32 v20, v23
	v_lshlrev_b32_e32 v19, 3, v87
	v_mad_u64_u32 v[20:21], s[70:71], v21, s39, v[20:21]
	v_and_b32_e32 v19, 24, v19
	v_mov_b32_e32 v23, v20
	v_lshlrev_b32_e32 v74, 1, v19
	v_lshl_add_u64 v[20:21], v[22:23], 0, v[74:75]
	v_add_co_u32_e32 v20, vcc, s50, v20
	v_lshlrev_b32_e32 v24, 7, v24
	s_nop 0
	v_addc_co_u32_e32 v21, vcc, 0, v21, vcc
	global_load_dwordx4 v[20:23], v[20:21], off offset:3584
	v_lshlrev_b32_e32 v19, 2, v19
	v_add3_u32 v19, 0, v24, v19
